# p_mix: 128 instead of 96 workgroups start with next-layer weight-conversion tickets; on top of the K-loop peel
# speedup vs baseline: 1.0064x; 1.0003x over previous
.LBB0_511:
	v_readlane_b32 s0, v254, 9
	s_mov_b32 s1, -1
	s_nop 0
	v_mbcnt_lo_u32_b32 v0, s1, 0
	v_mbcnt_hi_u32_b32 v0, s1, v0
	v_lshl_add_u32 v186, s0, 6, v0
	v_readlane_b32 s0, v254, 53
	v_readlane_b32 s1, v254, 54
	s_lshl_b32 s26, s0, 6
	s_mov_b32 s2, s0
	s_lshl_b64 s[4:5], s[26:27], 2
	v_readlane_b32 s0, v255, 0
	v_readlane_b32 s1, v255, 1
	s_add_u32 s0, s0, s4
	v_writelane_b32 v255, s4, 8
	s_addc_u32 s1, s1, s5
	s_add_u32 s0, s0, 0x9000
	v_writelane_b32 v255, s5, 9
	s_addc_u32 s1, s1, 0
	s_add_i32 s4, s2, 1
	v_writelane_b32 v255, s0, 10
	s_cmp_lg_u32 s2, 3
	s_cselect_b64 s[2:3], -1, 0
	v_writelane_b32 v255, s1, 11
	s_sub_i32 s0, s14, 64
	s_cmpk_lt_u32 s0, 0x80
	v_writelane_b32 v255, s2, 12
	s_cselect_b64 s[0:1], -1, 0
	v_cmp_eq_u32_e64 s[36:37], 0, v186
	v_writelane_b32 v255, s3, 13
	v_writelane_b32 v255, s0, 14
	s_nop 1
	v_writelane_b32 v255, s1, 15
	s_and_b64 s[0:1], s[2:3], s[0:1]
	s_andn2_b64 vcc, exec, s[0:1]
	s_mul_hi_u32 s0, s4, 0xbd00000
	v_writelane_b32 v255, s0, 16
	s_mul_i32 s0, s4, 0xbd00000
	v_writelane_b32 v255, s0, 17
	s_mul_hi_u32 s0, s4, 0x2b00000
	v_writelane_b32 v255, s0, 18
	s_mul_i32 s0, s4, 0x2b00000
	v_writelane_b32 v255, s0, 19
	s_mul_hi_u32 s0, s4, 0x5600000
	v_writelane_b32 v255, s0, 20
	s_mul_i32 s0, s4, 0x5600000
	v_writelane_b32 v255, s0, 21
	s_mul_hi_u32 s0, s4, 0x4ea0000
	v_writelane_b32 v255, s0, 22
	s_mov_b32 s0, s4
	v_writelane_b32 v255, s0, 23
	s_nop 1
	v_writelane_b32 v255, s1, 24
	s_mul_i32 s0, s4, 0x4ea0000
	v_writelane_b32 v255, s0, 25
	s_cbranch_vccnz .LBB0_701
	v_readlane_b32 s0, v254, 44
	s_add_i32 s20, s47, s0
	v_readlane_b32 s0, v255, 2
	v_readlane_b32 s1, v255, 17
	s_add_u32 s21, s0, s1
	v_readlane_b32 s0, v255, 4
	v_readlane_b32 s1, v255, 16
	s_addc_u32 s31, s0, s1
	s_add_u32 s34, s21, 0xa780000
	v_readlane_b32 s0, v254, 46
	s_addc_u32 s35, s31, 0
	s_lshl_b32 s0, s0, 1
	v_readlane_b32 s6, v255, 23
	s_add_u32 s38, s34, s0
	v_readlane_b32 s7, v255, 24
	s_addc_u32 s39, s35, 0
	s_mov_b32 s7, s27
	s_add_u32 s40, s21, 0x7c80000
	s_addc_u32 s41, s31, 0
	s_lshl_b64 s[2:3], s[6:7], 13
	s_lshl_b64 s[4:5], s[6:7], 24
	s_add_u32 s42, s21, 0x7480000
	s_addc_u32 s43, s31, 0
	s_mov_b32 s0, s6
	s_lshl_b64 s[6:7], s[6:7], 23
	s_add_u32 s44, s21, 0x7080000
	s_addc_u32 s45, s31, 0
	s_add_u32 s46, s21, 0x6880000
	s_addc_u32 s47, s31, 0
	s_add_u32 s48, s21, 0x4080000
	s_addc_u32 s49, s31, 0
	v_writelane_b32 v255, s0, 23
	s_add_u32 s50, s21, 0x2b00000
	s_addc_u32 s51, s31, 0
	v_writelane_b32 v255, s1, 24
	s_branch .LBB0_515
